# stack10 + attention unit prologue: bias-table load, Q loads and first-tile DMA issued together, consumed with counted vmcnt (one round trip instead of three)
# baseline (speedup 1.0000x reference)
; #define GAS __attribute__((address_space(1)))
; #define LAS __attribute__((address_space(3)))
; __device__ __forceinline__ int swap23(int i) { return (i & 0x13) | ((i & 4) << 1) | ((i & 8) >> 1); }
; __device__ __forceinline__ unsigned tr_off(int lane, int c, int t) { const int h = lane >> 5, blk = (lane >> 4) & 1, q = (lane & 15) >> 2, p = lane & 3; return offb(8 * h + 4 * t + q, 4 * c + 2 * blk + (p >> 1)) + 8u * (unsigned)(p & 1); }
; #define ATT_DMA(t, sb_) do { const size_t ko_ = (size_t)(t) * 64 * LDP; \
;         glds16_asm(k0src + ko_, (sb_) + wid * 1024); glds16_asm(k1src + ko_, (sb_) + 8192 + wid * 1024); glds16_asm(vsrc[0] + ko_, (sb_) + 16384 + wid * 2048); glds16_asm(vsrc[1] + ko_, (sb_) + 16384 + wid * 2048 + 1024); } while (0)
; __device__ __forceinline__ void attn_unit(LAS unsigned char* lds, const bf16* proj, bf16* Y, const float* relb, const float* hgain, float lam, float oscale, int b, int h, int qb, int tid, int lane, int wid, Stopwatch& sw) {
;     ...
;     LAS float* tab = (LAS float*)(lds + 98304);
;     if (tid < 129) tab[tid] = relb[t5_bucket(tid) * 8 + h] * LOG2E;
;     const float bias31 = relb[31 * 8 + h] * LOG2E;
;     LAS unsigned char* qlds = lds + 100352 + wid * 4096 + hi * 512 + r32 * 16;
;     { const bf16* qp = proj + (rowbase + qw + r32) * LDP + C_QD + h * 128 + mp * 64 + hi * 8;
; #pragma unroll
;       for (int d0 = 0; d0 < 4; ++d0) *(LAS bf16x8*)(qlds + d0 * 1024) = *(const GAS bf16x8*)(qp + d0 * 16); }
;     const bf16* k0src = proj + (rowbase + (lane & 32) + swap23(r32)) * LDP + C_KD + h * 128 + wid * 8;
;     const bf16* k1src = k0src + 64;
;     const bf16* vsrc[2];
; #pragma unroll
;     for (int i = 0; i < 2; ++i) { const int vrow = 8 * wid + 4 * i + (lane >> 4); const int ch = (lane & 15) ^ (((vrow & 3) << 2) | ((vrow >> 2) & 3)); vsrc[i] = proj + (rowbase + vrow) * LDP + C_VD + h * 128 + ch * 8; }
;     ...
;     unsigned va[4][2];
; #pragma unroll
;     for (int c = 0; c < 4; ++c) { va[c][0] = 16384u + tr_off(lane, c, 0); va[c][1] = 16384u + tr_off(lane, c, 1); }
;     const unsigned kboff = mp * 8192 + hi * 1024 + r32 * 16;
;     const int NT = 2 * qb + 2;
;     ATT_DMA(0, lds); ATT_DMA(1, lds + 32768);
.LBB0_359:
	s_or_b64 exec, exec, s[38:39]
	v_lshl_or_b32 v4, v2, 3, s0
	v_readlane_b32 s40, v250, 2
	v_ashrrev_i32_e32 v5, 31, v4
	v_readlane_b32 s42, v250, 4
	v_readlane_b32 s43, v250, 5
	v_readlane_b32 s41, v250, 3
	v_readlane_b32 s44, v250, 6
	v_lshl_add_u64 v[4:5], v[4:5], 2, s[42:43]
	global_load_dword v210, v[4:5], off
	v_lshl_add_u32 v211, v61, 2, 0
	v_add_u32_e32 v211, 0x18000, v211
	v_readlane_b32 s45, v250, 7
	v_readlane_b32 s46, v250, 8
	v_readlane_b32 s47, v250, 9
	v_readlane_b32 s48, v250, 10
	v_readlane_b32 s49, v250, 11
	v_readlane_b32 s50, v250, 12
	v_readlane_b32 s51, v250, 13
	v_readlane_b32 s52, v250, 14
	v_readlane_b32 s53, v250, 15
	v_readlane_b32 s54, v250, 16
	v_readlane_b32 s55, v250, 17
.LBB0_360:
	s_or_b64 exec, exec, s[36:37]
	s_ashr_i32 s24, s3, 6
	s_lshl_b32 s5, s19, 7
	v_readlane_b32 s3, v252, 60
	v_and_b32_e32 v60, 31, v61
	s_or_b32 s16, s5, s3
	s_ashr_i32 s25, s24, 31
	s_lshl_b64 s[36:37], s[24:25], 12
	v_or_b32_e32 v64, s16, v60
	v_or_b32_e32 v151, s36, v64
	v_mov_b64_e32 v[20:21], s[12:13]
	v_mad_u64_u32 v[4:5], s[24:25], v151, s33, v[20:21]
	s_lshl_b32 s3, s0, 2
	v_readlane_b32 s40, v250, 2
	v_mad_i32_i24 v5, s37, v239, v5
	s_lshl_b32 s34, s0, 8
	v_bfe_u32 v44, v61, 5, 1
	v_mov_b32_e32 v2, s3
	v_readlane_b32 s42, v250, 4
	v_readlane_b32 s43, v250, 5
	v_lshl_add_u64 v[4:5], v[4:5], 0, s[34:35]
	s_lshl_b32 s24, s31, 1
	s_mov_b32 s25, s35
	v_lshl_add_u64 v[4:5], v[4:5], 0, s[24:25]
	s_movk_i32 s3, 0x3000
	global_load_dword v34, v2, s[42:43] offset:992
	v_lshlrev_b32_e32 v2, 4, v44
	v_lshl_add_u64 v[4:5], v[4:5], 0, v[2:3]
	s_mov_b64 s[24:25], 0x3800
	v_add_co_u32_e32 v16, vcc, s3, v4
	v_lshl_add_u64 v[12:13], v[4:5], 0, s[24:25]
	s_nop 0
	v_addc_co_u32_e32 v17, vcc, 0, v5, vcc
	global_load_dwordx4 v[4:7], v[12:13], off offset:32
	global_load_dwordx4 v[8:11], v[12:13], off offset:64
	s_nop 0
	global_load_dwordx4 v[12:15], v[12:13], off offset:96
	s_nop 0
	global_load_dwordx4 v[16:19], v[16:17], off offset:2048
	v_bfe_u32 v26, v61, 4, 2
	v_readlane_b32 s3, v252, 58
	v_lshlrev_b32_e32 v22, 1, v61
	v_lshrrev_b32_e32 v63, 1, v61
	v_and_b32_e32 v24, 51, v61
	v_readlane_b32 s18, v252, 61
	v_and_b32_e32 v28, 15, v61
	v_lshl_add_u32 v30, v44, 9, s3
	v_lshlrev_b32_e32 v31, 4, v60
	v_lshlrev_b32_e32 v35, 2, v26
	v_readlane_b32 s3, v252, 59
	v_and_b32_e32 v32, 8, v22
	v_and_or_b32 v24, v63, 4, v24
	v_or_b32_e32 v22, s18, v26
	v_lshlrev_b32_e32 v33, 10, v44
	v_add_u32_e32 v62, v30, v31
	v_bitop3_b32 v30, v35, v28, s3 bitop3:0x36
	v_readlane_b32 s3, v252, 62
	v_mov_b32_e32 v23, v3
	v_mov_b32_e32 v27, v3
	v_or_b32_e32 v26, 4, v22
	v_lshrrev_b32_e32 v164, 1, v60
	v_xor_b32_e32 v164, v164, v44
	v_and_b32_e32 v164, 1, v164
	v_lshlrev_b32_e32 v164, 4, v164
	v_bfe_u32 v206, v60, 2, 2
	v_lshl_or_b32 v164, v206, 5, v164
	v_lshl_or_b32 v164, v60, 7, v164
	v_or_b32_e32 v164, s3, v164
	v_or3_b32 v31, v24, v32, s36
	v_lshl_add_u64 v[22:23], s[36:37], 0, v[22:23]
	v_lshlrev_b32_e32 v24, 4, v30
	v_bfe_u32 v36, v26, 2, 2
	v_lshl_add_u64 v[26:27], s[36:37], 0, v[26:27]
	v_mad_u64_u32 v[30:31], s[24:25], v31, s33, v[20:21]
	v_mad_u64_u32 v[32:33], s[24:25], v22, s33, v[20:21]
	v_bitop3_b32 v22, v36, v28, v35 bitop3:0x36
	v_mad_u64_u32 v[20:21], s[24:25], v26, s33, v[20:21]
	v_mad_i32_i24 v31, s37, v239, v31
	s_lshl_b32 s38, s18, 1
	s_mov_b32 s39, s35
	v_mad_i32_i24 v33, v23, s33, v33
	v_mad_i32_i24 v21, v27, s33, v21
	v_lshlrev_b32_e32 v28, 4, v22
	v_lshl_add_u64 v[22:23], v[30:31], 0, s[34:35]
	v_mov_b32_e32 v25, v3
	v_mov_b32_e32 v29, v3
	v_lshl_add_u64 v[26:27], v[32:33], 0, s[34:35]
	v_lshl_add_u64 v[20:21], v[20:21], 0, s[34:35]
	v_lshl_add_u64 v[22:23], v[22:23], 0, s[38:39]
	v_and_b32_e32 v206, 63, v61
	v_lshrrev_b32_e32 v207, 3, v206
	v_add_u32_e32 v207, s18, v207
	v_and_b32_e32 v208, 0x33, v207
	v_lshlrev_b32_e32 v209, 1, v207
	v_and_b32_e32 v209, 8, v209
	v_or_b32_e32 v208, v208, v209
	v_lshrrev_b32_e32 v209, 1, v207
	v_and_b32_e32 v209, 4, v209
	v_or_b32_e32 v208, v208, v209
	v_add_u32_e32 v208, s36, v208
	v_lshrrev_b32_e32 v209, 1, v207
	v_and_b32_e32 v209, 7, v209
	v_and_b32_e32 v206, 7, v206
	v_xor_b32_e32 v206, v206, v209
	v_lshlrev_b32_e32 v206, 4, v206
	v_add_u32_e32 v206, s34, v206
	v_mov_b32_e32 v207, 0
	v_lshl_add_u64 v[206:207], s[12:13], 0, v[206:207]
	v_mad_u64_u32 v[22:23], s[100:101], v208, s33, v[206:207]
	s_mov_b64 s[24:25], 0x4000
	v_lshl_add_u64 v[24:25], v[26:27], 0, v[24:25]
	v_lshl_add_u64 v[20:21], v[20:21], 0, v[28:29]
	v_lshl_add_u64 v[52:53], v[22:23], 0, s[24:25]
	s_mov_b64 s[24:25], 0x4800
	v_lshl_add_u64 v[54:55], v[24:25], 0, s[24:25]
	v_lshl_add_u64 v[58:59], v[20:21], 0, s[24:25]
	s_mov_b64 s[24:25], 0x4080
	v_readlane_b32 s18, v253, 3
	v_lshl_add_u64 v[56:57], v[22:23], 0, s[24:25]
	s_mov_b32 s3, m0
	s_mov_b32 m0, s18
	s_nop 0
	global_load_lds_dwordx4 v[52:53], off
	s_mov_b32 m0, s3
	v_readlane_b32 s18, v252, 63
	s_mov_b32 s3, m0
	s_mov_b32 m0, s18
	s_nop 0
	global_load_lds_dwordx4 v[56:57], off
	s_mov_b32 m0, s3
	v_readlane_b32 s18, v253, 0
	s_mov_b32 s3, m0
	s_mov_b32 m0, s18
	s_nop 0
	global_load_lds_dwordx4 v[54:55], off
	s_mov_b32 m0, s3
	s_mov_b64 s[24:25], 0x1c4000
	v_readlane_b32 s18, v253, 1
	s_mov_b32 s3, m0
	s_mov_b32 m0, s18
	s_nop 0
	global_load_lds_dwordx4 v[58:59], off
	s_mov_b32 m0, s3
	v_lshl_add_u64 v[26:27], v[22:23], 0, s[24:25]
	s_mov_b64 s[24:25], 0x1c4080
	v_readlane_b32 s18, v253, 2
	s_mov_b32 s3, m0
	s_mov_b32 m0, s18
	s_nop 0
	global_load_lds_dwordx4 v[26:27], off
	s_mov_b32 m0, s3
	v_lshl_add_u64 v[22:23], v[22:23], 0, s[24:25]
	s_mov_b64 s[24:25], 0x1c4800
	v_readlane_b32 s18, v253, 4
	s_mov_b32 s3, m0
	s_mov_b32 m0, s18
	s_nop 0
	global_load_lds_dwordx4 v[22:23], off
	s_mov_b32 m0, s3
	v_lshl_add_u64 v[24:25], v[24:25], 0, s[24:25]
	v_readlane_b32 s18, v253, 5
	s_mov_b32 s3, m0
	s_mov_b32 m0, s18
	s_nop 0
	global_load_lds_dwordx4 v[24:25], off
	s_mov_b32 m0, s3
	v_lshl_add_u64 v[20:21], v[20:21], 0, s[24:25]
	v_readlane_b32 s18, v253, 6
	s_mov_b32 s3, m0
	s_mov_b32 m0, s18
	s_nop 0
	global_load_lds_dwordx4 v[20:21], off
	s_mov_b32 m0, s3
	s_waitcnt vmcnt(11)
	ds_write_b128 v62, v[4:7] offset:1024
	s_waitcnt vmcnt(10)
	ds_write_b128 v62, v[8:11] offset:2048
	s_waitcnt vmcnt(9)
	ds_write_b128 v62, v[12:15] offset:3072
	s_waitcnt vmcnt(8)
	ds_write_b128 v62, v[16:19]
	s_movk_i32 s100, 0x81
	v_cmp_gt_i32_e32 vcc, s100, v61
	s_and_saveexec_b64 s[100:101], vcc
	v_mul_f32_e32 v210, 0x3fb8aa3b, v210
	ds_write_b32 v211, v210
	ds_write_b32 v211, v210 offset:35200
	s_or_b64 exec, exec, s[100:101]
	v_mul_f32_e32 v204, 0x3fb8aa3b, v34
	v_cmp_gt_u32_e32 vcc, 0x60, v61
	v_add_u32_e32 v205, 0x81, v61
	s_nop 0
	v_cndmask_b32_e32 v204, v204, v246, vcc
	v_cndmask_b32_e32 v205, v205, v61, vcc
	v_lshlrev_b32_e32 v205, 2, v205
	v_add_u32_e32 v205, 0x20800, v205
	v_cmp_gt_u32_e32 vcc, 0xbf, v61
	s_and_saveexec_b64 s[100:101], vcc
	ds_write_b32 v205, v204
	s_or_b64 exec, exec, s[100:101]
	s_waitcnt vmcnt(0) lgkmcnt(0)
	s_barrier
; #define TS_END(sw, id) do { if ((id) == TSSEL && (sw).on) (sw).acc += __builtin_amdgcn_s_memrealtime() - (sw).t0; } while (0)
; #define TS_END(sw, id) do { } while (0)
; #define WG_BAR() do { asm volatile("s_waitcnt vmcnt(0) lgkmcnt(0)" ::: "memory"); __builtin_amdgcn_s_barrier(); asm volatile("" ::: "memory"); } while (0)
; #define ATT_QK(S0, S1, sbp, cin) do { S0 = splat16(cin); S1 = S0; \
;         _Pragma("unroll") for (int d0 = 0; d0 < 4; ++d0) { const bf16x8 kf0_ = *(const LAS bf16x8*)((sbp) + kboff + d0 * 2048), kf1_ = *(const LAS bf16x8*)((sbp) + kboff + d0 * 2048 + 512), q_ = *(const LAS bf16x8*)(qlds + d0 * 1024); \
;             S0 = MFMA32(kf0_, q_, S0); S1 = MFMA32(kf1_, q_, S1); } } while (0)
; __device__ __forceinline__ void attn_unit(LAS unsigned char* lds, const bf16* proj, bf16* Y, const float* relb, const float* hgain, float lam, float oscale, int b, int h, int qb, int tid, int lane, int wid, Stopwatch& sw) {
;     ...
;     WG_BAR();
;     TS_END(sw, 8);
;     f32x16 sA0, sA1, sB0, sB1;
;     typedef __bf16 bf2_t_ __attribute__((ext_vector_type(2)));
;     const bf2_t_ one2 = __builtin_bit_cast(bf2_t_, 0x3F803F80u);
;     { const bool far0 = (63 + 128 <= qw); ATT_QK(sA0, sA1, lds, far0 ? bias31 : 0.f);
;       if (!far0) {
; #pragma unroll
;           for (int r = 0; r < 16; ++r) { const int key = 16 * (r >> 3) + 8 * hi + (r & 7); const int d0_ = qi - key, d1_ = d0_ - 32;
;               const float b0 = tab[d0_ < 0 ? 0 : (d0_ > 128 ? 128 : d0_)], b1 = tab[d1_ < 0 ? 0 : (d1_ > 128 ? 128 : d1_)];
;               sA0[r] = d0_ < 0 ? -1e30f : sA0[r] + b0; sA1[r] = d1_ < 0 ? -1e30f : sA1[r] + b1; } }
	v_add_u32_e32 v45, 0, v164
	v_xor_b32_e32 v206, 32, v45
	v_xor_b32_e32 v207, 64, v45
	v_xor_b32_e32 v208, 0x60, v45
	ds_read_b128 v[36:39], v45
	ds_read_b128 v[40:43], v62
	s_cmpk_gt_u32 s16, 0xbe
	v_mul_f32_e32 v165, 0x3fb8aa3b, v34
	s_cselect_b64 vcc, -1, 0
	v_cndmask_b32_e32 v4, 0, v165, vcc
	v_mov_b32_e32 v5, v4
	v_mov_b32_e32 v6, v4
	v_mov_b32_e32 v7, v4
	v_mov_b32_e32 v8, v4
	v_mov_b32_e32 v9, v4
	v_mov_b32_e32 v10, v4
	v_mov_b32_e32 v11, v4
	v_mov_b32_e32 v12, v4
	v_mov_b32_e32 v13, v4
	v_mov_b32_e32 v14, v4
	v_mov_b32_e32 v15, v4
	v_mov_b32_e32 v16, v4
	v_mov_b32_e32 v17, v4
	v_mov_b32_e32 v18, v4
	v_mov_b32_e32 v19, v4
	v_mov_b32_e32 v163, s37
	v_lshlrev_b32_e32 v150, 3, v44
	s_waitcnt lgkmcnt(0)
	v_mfma_f32_32x32x16_bf16 v[20:35], v[36:39], v[40:43], v[4:19]
	ds_read_b128 v[36:39], v45 offset:4096
	s_and_b64 vcc, exec, vcc
	v_readlane_b32 s41, v250, 3
	v_readlane_b32 s44, v250, 6
	v_readlane_b32 s45, v250, 7
	v_readlane_b32 s46, v250, 8
	v_readlane_b32 s47, v250, 9
	s_waitcnt lgkmcnt(0)
	v_mfma_f32_32x32x16_bf16 v[4:19], v[36:39], v[40:43], v[4:19]
	ds_read_b128 v[36:39], v206
	ds_read_b128 v[40:43], v62 offset:1024
	v_readlane_b32 s48, v250, 10
	v_readlane_b32 s49, v250, 11
	v_readlane_b32 s50, v250, 12
	v_readlane_b32 s51, v250, 13
	v_readlane_b32 s52, v250, 14
	v_readlane_b32 s53, v250, 15
	s_waitcnt lgkmcnt(0)
	v_mfma_f32_32x32x16_bf16 v[20:35], v[36:39], v[40:43], v[20:35]
	ds_read_b128 v[36:39], v206 offset:4096
	v_readlane_b32 s54, v250, 16
	v_readlane_b32 s55, v250, 17
	s_waitcnt lgkmcnt(0)
	v_mfma_f32_32x32x16_bf16 v[4:19], v[36:39], v[40:43], v[4:19]
	ds_read_b128 v[36:39], v207
	ds_read_b128 v[40:43], v62 offset:2048
	s_waitcnt lgkmcnt(0)
	v_mfma_f32_32x32x16_bf16 v[20:35], v[36:39], v[40:43], v[20:35]
	ds_read_b128 v[36:39], v207 offset:4096
	s_waitcnt lgkmcnt(0)
	v_mfma_f32_32x32x16_bf16 v[4:19], v[36:39], v[40:43], v[4:19]
	ds_read_b128 v[36:39], v208
	ds_read_b128 v[40:43], v62 offset:3072
	s_waitcnt lgkmcnt(0)
	v_mfma_f32_32x32x16_bf16 v[20:35], v[36:39], v[40:43], v[20:35]
	ds_read_b128 v[36:39], v208 offset:4096
	s_waitcnt lgkmcnt(0)
	v_mfma_f32_32x32x16_bf16 v[4:19], v[36:39], v[40:43], v[4:19]
	s_cbranch_vccnz .LBB0_394
	v_sub_u32_e32 v38, v64, v150
	v_min_i32_e32 v36, 0xa0, v38
	v_subrev_u32_e32 v36, 32, v36
	v_cmp_gt_i32_e32 vcc, 32, v38
	v_cmp_lt_i32_e64 s[36:37], -1, v38
	v_mov_b32_e32 v37, 0xf149f2ca
	v_cndmask_b32_e64 v36, v36, 0, vcc
	v_lshl_add_u32 v36, v36, 2, 0
	v_add_u32_e32 v36, 0x18000, v36
	ds_read_b32 v65, v36
	v_mov_b32_e32 v36, 0xf149f2ca
	s_and_saveexec_b64 s[38:39], s[36:37]
	s_cbranch_execz .LBB0_363
	v_min_u32_e32 v36, 0x80, v38
	v_lshl_add_u32 v36, v36, 2, 0
	v_add_u32_e32 v36, 0x18000, v36
	ds_read_b32 v36, v36
	s_waitcnt lgkmcnt(0)
	v_add_f32_e32 v36, v20, v36
